# norm2 / post_norm: the five vector loads of a modulation-row change issued together (one wait instead of three round trips)
# baseline (speedup 1.0000x reference)
.LBB0_762:
	s_andn2_b64 vcc, exec, s[6:7]
	s_cbranch_vccnz .LBB0_834
	v_readfirstlane_b32 s16, v0
	s_lshr_b32 s16, s16, 6
	s_lshl_b32 s17, s2, 3
	s_add_u32 s16, s16, s17
	s_lshl_b32 s17, s82, 3
	s_add_u32 s18, s96, s17
	s_sub_u32 s18, s18, 1
	v_cvt_f32_u32_e32 v136, s17
	v_cvt_f32_u32_e32 v137, s18
	v_rcp_iflag_f32_e32 v136, v136
	s_nop 0
	v_mul_f32_e32 v136, v137, v136
	v_cvt_u32_f32_e32 v136, v136
	s_nop 0
	v_readfirstlane_b32 s19, v136
	s_mul_i32 s12, s19, s17
	s_cmp_gt_u32 s12, s18
	s_cselect_b32 s13, 1, 0
	s_sub_u32 s19, s19, s13
	s_add_u32 s12, s19, 1
	s_mul_i32 s12, s12, s17
	s_cmp_le_u32 s12, s18
	s_cselect_b32 s13, 1, 0
	s_add_u32 s19, s19, s13
	s_mul_i32 s12, s16, s19
	s_cmp_ge_u32 s12, s96
	s_cbranch_scc1 .Lpq_end
	s_add_u32 s13, s12, s19
	s_min_u32 s13, s13, s96
	v_readlane_b32 s4, v252, 4
	v_readlane_b32 s5, v252, 5
	v_readlane_b32 s14, v255, 34
	s_sub_u32 s4, s4, 0x18
	s_subb_u32 s5, s5, 0
	s_load_dwordx2 s[4:5], s[4:5], 0x0
	v_and_b32_e32 v2, 63, v0
	v_lshlrev_b32_e32 v3, 4, v2
	v_lshlrev_b32_e32 v160, 5, v2
	v_add_u32_e32 v161, 0x1000, v160
	s_mul_i32 s16, s14, 0x3c000
	s_mul_i32 s17, s14, 0xc000
	s_lshl_b32 s18, s14, 13
	v_readlane_b32 s48, v252, 16
	v_readlane_b32 s49, v252, 17
	v_readlane_b32 s50, v252, 20
	v_readlane_b32 s51, v252, 21
	s_waitcnt lgkmcnt(0)
	s_add_u32 s38, s4, 0x15000000
	s_addc_u32 s39, s5, 0
	s_add_u32 s42, s4, 0x1b200000
	s_addc_u32 s43, s5, 0
	s_add_u32 s46, s4, 0x10000
	s_addc_u32 s47, s5, 0
	s_add_u32 s46, s46, s16
	s_addc_u32 s47, s47, 0
	s_add_u32 s48, s48, s17
	s_addc_u32 s49, s49, 0
	s_add_u32 s50, s50, s18
	s_addc_u32 s51, s51, 0
	s_mov_b32 s15, -1
	s_lshl_b32 s16, s12, 12
	s_add_u32 s52, s38, s16
	s_addc_u32 s53, s39, 0
	global_load_dwordx4 v[102:105], v3, s[52:53]
	global_load_dwordx4 v[106:109], v3, s[52:53] offset:1024
	global_load_dwordx4 v[110:113], v3, s[52:53] offset:2048
	global_load_dwordx4 v[114:117], v3, s[52:53] offset:3072
	s_add_u32 s18, s12, 1
	s_sub_u32 s19, s13, 1
	s_min_u32 s18, s18, s19
	s_lshl_b32 s16, s18, 12
	s_add_u32 s52, s38, s16
	s_addc_u32 s53, s39, 0
	global_load_dwordx4 v[118:121], v3, s[52:53]
	global_load_dwordx4 v[122:125], v3, s[52:53] offset:1024
	global_load_dwordx4 v[126:129], v3, s[52:53] offset:2048
	global_load_dwordx4 v[130:133], v3, s[52:53] offset:3072
	s_lshr_b32 s16, s12, 12
	s_cmp_lt_u32 s12, 0x4000
	s_cselect_b32 s16, s16, 4
	s_cmp_eq_u32 s16, s15
	s_cbranch_scc1 .Lpq_mod_ok_a
	s_mov_b32 s15, s16
	s_mul_i32 s16, s16, 0xc000
	s_add_u32 s52, s46, s16
	s_addc_u32 s53, s47, 0
	s_add_u32 s10, s52, 0x8000
	s_addc_u32 s11, s53, 0
	s_add_u32 s52, s52, 0x6000
	s_addc_u32 s53, s53, 0
	s_add_u32 s16, s48, 0x8000
	s_addc_u32 s17, s49, 0
	s_add_u32 s18, s48, 0x6000
	s_addc_u32 s19, s49, 0
	global_load_dwordx4 v[6:9], v160, s[10:11]
	global_load_dwordx4 v[70:73], v160, s[16:17]
	global_load_dwordx4 v[38:41], v160, s[52:53]
	global_load_dwordx4 v[216:219], v160, s[50:51]
	global_load_dwordx4 v[176:179], v160, s[18:19]
	global_load_dwordx4 v[10:13], v160, s[10:11] offset:16
	global_load_dwordx4 v[74:77], v160, s[16:17] offset:16
	global_load_dwordx4 v[42:45], v160, s[52:53] offset:16
	global_load_dwordx4 v[220:223], v160, s[50:51] offset:16
	global_load_dwordx4 v[180:183], v160, s[18:19] offset:16
	global_load_dwordx4 v[14:17], v160, s[10:11] offset:2048
	global_load_dwordx4 v[78:81], v160, s[16:17] offset:2048
	global_load_dwordx4 v[46:49], v160, s[52:53] offset:2048
	global_load_dwordx4 v[224:227], v160, s[50:51] offset:2048
	global_load_dwordx4 v[184:187], v160, s[18:19] offset:2048
	global_load_dwordx4 v[18:21], v160, s[10:11] offset:2064
	global_load_dwordx4 v[82:85], v160, s[16:17] offset:2064
	global_load_dwordx4 v[50:53], v160, s[52:53] offset:2064
	global_load_dwordx4 v[228:231], v160, s[50:51] offset:2064
	global_load_dwordx4 v[188:191], v160, s[18:19] offset:2064
	global_load_dwordx4 v[22:25], v161, s[10:11]
	global_load_dwordx4 v[86:89], v161, s[16:17]
	global_load_dwordx4 v[54:57], v161, s[52:53]
	global_load_dwordx4 v[232:235], v161, s[50:51]
	global_load_dwordx4 v[192:195], v161, s[18:19]
	global_load_dwordx4 v[26:29], v161, s[10:11] offset:16
	global_load_dwordx4 v[90:93], v161, s[16:17] offset:16
	global_load_dwordx4 v[58:61], v161, s[52:53] offset:16
	global_load_dwordx4 v[236:239], v161, s[50:51] offset:16
	global_load_dwordx4 v[196:199], v161, s[18:19] offset:16
	global_load_dwordx4 v[30:33], v161, s[10:11] offset:2048
	global_load_dwordx4 v[94:97], v161, s[16:17] offset:2048
	global_load_dwordx4 v[62:65], v161, s[52:53] offset:2048
	global_load_dwordx4 v[240:243], v161, s[50:51] offset:2048
	global_load_dwordx4 v[162:165], v161, s[18:19] offset:2048
	global_load_dwordx4 v[34:37], v161, s[10:11] offset:2064
	global_load_dwordx4 v[98:101], v161, s[16:17] offset:2064
	global_load_dwordx4 v[66:69], v161, s[52:53] offset:2064
	global_load_dwordx4 v[244:247], v161, s[50:51] offset:2064
	global_load_dwordx4 v[166:169], v161, s[18:19] offset:2064
	s_waitcnt vmcnt(0)
	v_pk_add_f32 v[6:7], v[6:7], v[70:71]
	v_pk_add_f32 v[6:7], v[6:7], 1.0 op_sel_hi:[1,0]
	v_pk_add_f32 v[8:9], v[8:9], v[72:73]
	v_pk_add_f32 v[8:9], v[8:9], 1.0 op_sel_hi:[1,0]
	v_pk_add_f32 v[10:11], v[10:11], v[74:75]
	v_pk_add_f32 v[10:11], v[10:11], 1.0 op_sel_hi:[1,0]
	v_pk_add_f32 v[12:13], v[12:13], v[76:77]
	v_pk_add_f32 v[12:13], v[12:13], 1.0 op_sel_hi:[1,0]
	v_pk_add_f32 v[14:15], v[14:15], v[78:79]
	v_pk_add_f32 v[14:15], v[14:15], 1.0 op_sel_hi:[1,0]
	v_pk_add_f32 v[16:17], v[16:17], v[80:81]
	v_pk_add_f32 v[16:17], v[16:17], 1.0 op_sel_hi:[1,0]
	v_pk_add_f32 v[18:19], v[18:19], v[82:83]
	v_pk_add_f32 v[18:19], v[18:19], 1.0 op_sel_hi:[1,0]
	v_pk_add_f32 v[20:21], v[20:21], v[84:85]
	v_pk_add_f32 v[20:21], v[20:21], 1.0 op_sel_hi:[1,0]
	v_pk_add_f32 v[22:23], v[22:23], v[86:87]
	v_pk_add_f32 v[22:23], v[22:23], 1.0 op_sel_hi:[1,0]
	v_pk_add_f32 v[24:25], v[24:25], v[88:89]
	v_pk_add_f32 v[24:25], v[24:25], 1.0 op_sel_hi:[1,0]
	v_pk_add_f32 v[26:27], v[26:27], v[90:91]
	v_pk_add_f32 v[26:27], v[26:27], 1.0 op_sel_hi:[1,0]
	v_pk_add_f32 v[28:29], v[28:29], v[92:93]
	v_pk_add_f32 v[28:29], v[28:29], 1.0 op_sel_hi:[1,0]
	v_pk_add_f32 v[30:31], v[30:31], v[94:95]
	v_pk_add_f32 v[30:31], v[30:31], 1.0 op_sel_hi:[1,0]
	v_pk_add_f32 v[32:33], v[32:33], v[96:97]
	v_pk_add_f32 v[32:33], v[32:33], 1.0 op_sel_hi:[1,0]
	v_pk_add_f32 v[34:35], v[34:35], v[98:99]
	v_pk_add_f32 v[34:35], v[34:35], 1.0 op_sel_hi:[1,0]
	v_pk_add_f32 v[36:37], v[36:37], v[100:101]
	v_pk_add_f32 v[36:37], v[36:37], 1.0 op_sel_hi:[1,0]
	v_pk_mul_f32 v[6:7], v[216:217], v[6:7]
	v_pk_mul_f32 v[8:9], v[218:219], v[8:9]
	v_pk_mul_f32 v[10:11], v[220:221], v[10:11]
	v_pk_mul_f32 v[12:13], v[222:223], v[12:13]
	v_pk_mul_f32 v[14:15], v[224:225], v[14:15]
	v_pk_mul_f32 v[16:17], v[226:227], v[16:17]
	v_pk_mul_f32 v[18:19], v[228:229], v[18:19]
	v_pk_mul_f32 v[20:21], v[230:231], v[20:21]
	v_pk_mul_f32 v[22:23], v[232:233], v[22:23]
	v_pk_mul_f32 v[24:25], v[234:235], v[24:25]
	v_pk_mul_f32 v[26:27], v[236:237], v[26:27]
	v_pk_mul_f32 v[28:29], v[238:239], v[28:29]
	v_pk_mul_f32 v[30:31], v[240:241], v[30:31]
	v_pk_mul_f32 v[32:33], v[242:243], v[32:33]
	v_pk_mul_f32 v[34:35], v[244:245], v[34:35]
	v_pk_mul_f32 v[36:37], v[246:247], v[36:37]
	v_pk_add_f32 v[38:39], v[38:39], v[176:177]
	v_pk_add_f32 v[40:41], v[40:41], v[178:179]
	v_pk_add_f32 v[42:43], v[42:43], v[180:181]
	v_pk_add_f32 v[44:45], v[44:45], v[182:183]
	v_pk_add_f32 v[46:47], v[46:47], v[184:185]
	v_pk_add_f32 v[48:49], v[48:49], v[186:187]
	v_pk_add_f32 v[50:51], v[50:51], v[188:189]
	v_pk_add_f32 v[52:53], v[52:53], v[190:191]
	v_pk_add_f32 v[54:55], v[54:55], v[192:193]
	v_pk_add_f32 v[56:57], v[56:57], v[194:195]
	v_pk_add_f32 v[58:59], v[58:59], v[196:197]
	v_pk_add_f32 v[60:61], v[60:61], v[198:199]
	v_pk_add_f32 v[62:63], v[62:63], v[162:163]
	v_pk_add_f32 v[64:65], v[64:65], v[164:165]
	v_pk_add_f32 v[66:67], v[66:67], v[166:167]
	v_pk_add_f32 v[68:69], v[68:69], v[168:169]

.Lpq_loop:
	s_lshr_b32 s16, s12, 12
	s_cmp_lt_u32 s12, 0x4000
	s_cselect_b32 s16, s16, 4
	s_cmp_eq_u32 s16, s15
	s_cbranch_scc1 .Lpq_mod_ok_b
	s_mov_b32 s15, s16
	s_mul_i32 s16, s16, 0xc000
	s_add_u32 s52, s46, s16
	s_addc_u32 s53, s47, 0
	s_add_u32 s10, s52, 0x8000
	s_addc_u32 s11, s53, 0
	s_add_u32 s52, s52, 0x6000
	s_addc_u32 s53, s53, 0
	s_add_u32 s16, s48, 0x8000
	s_addc_u32 s17, s49, 0
	s_add_u32 s18, s48, 0x6000
	s_addc_u32 s19, s49, 0
	global_load_dwordx4 v[6:9], v160, s[10:11]
	global_load_dwordx4 v[70:73], v160, s[16:17]
	global_load_dwordx4 v[38:41], v160, s[52:53]
	global_load_dwordx4 v[216:219], v160, s[50:51]
	global_load_dwordx4 v[176:179], v160, s[18:19]
	global_load_dwordx4 v[10:13], v160, s[10:11] offset:16
	global_load_dwordx4 v[74:77], v160, s[16:17] offset:16
	global_load_dwordx4 v[42:45], v160, s[52:53] offset:16
	global_load_dwordx4 v[220:223], v160, s[50:51] offset:16
	global_load_dwordx4 v[180:183], v160, s[18:19] offset:16
	global_load_dwordx4 v[14:17], v160, s[10:11] offset:2048
	global_load_dwordx4 v[78:81], v160, s[16:17] offset:2048
	global_load_dwordx4 v[46:49], v160, s[52:53] offset:2048
	global_load_dwordx4 v[224:227], v160, s[50:51] offset:2048
	global_load_dwordx4 v[184:187], v160, s[18:19] offset:2048
	global_load_dwordx4 v[18:21], v160, s[10:11] offset:2064
	global_load_dwordx4 v[82:85], v160, s[16:17] offset:2064
	global_load_dwordx4 v[50:53], v160, s[52:53] offset:2064
	global_load_dwordx4 v[228:231], v160, s[50:51] offset:2064
	global_load_dwordx4 v[188:191], v160, s[18:19] offset:2064
	global_load_dwordx4 v[22:25], v161, s[10:11]
	global_load_dwordx4 v[86:89], v161, s[16:17]
	global_load_dwordx4 v[54:57], v161, s[52:53]
	global_load_dwordx4 v[232:235], v161, s[50:51]
	global_load_dwordx4 v[192:195], v161, s[18:19]
	global_load_dwordx4 v[26:29], v161, s[10:11] offset:16
	global_load_dwordx4 v[90:93], v161, s[16:17] offset:16
	global_load_dwordx4 v[58:61], v161, s[52:53] offset:16
	global_load_dwordx4 v[236:239], v161, s[50:51] offset:16
	global_load_dwordx4 v[196:199], v161, s[18:19] offset:16
	global_load_dwordx4 v[30:33], v161, s[10:11] offset:2048
	global_load_dwordx4 v[94:97], v161, s[16:17] offset:2048
	global_load_dwordx4 v[62:65], v161, s[52:53] offset:2048
	global_load_dwordx4 v[240:243], v161, s[50:51] offset:2048
	global_load_dwordx4 v[162:165], v161, s[18:19] offset:2048
	global_load_dwordx4 v[34:37], v161, s[10:11] offset:2064
	global_load_dwordx4 v[98:101], v161, s[16:17] offset:2064
	global_load_dwordx4 v[66:69], v161, s[52:53] offset:2064
	global_load_dwordx4 v[244:247], v161, s[50:51] offset:2064
	global_load_dwordx4 v[166:169], v161, s[18:19] offset:2064
	s_waitcnt vmcnt(0)
	v_pk_add_f32 v[6:7], v[6:7], v[70:71]
	v_pk_add_f32 v[6:7], v[6:7], 1.0 op_sel_hi:[1,0]
	v_pk_add_f32 v[8:9], v[8:9], v[72:73]
	v_pk_add_f32 v[8:9], v[8:9], 1.0 op_sel_hi:[1,0]
	v_pk_add_f32 v[10:11], v[10:11], v[74:75]
	v_pk_add_f32 v[10:11], v[10:11], 1.0 op_sel_hi:[1,0]
	v_pk_add_f32 v[12:13], v[12:13], v[76:77]
	v_pk_add_f32 v[12:13], v[12:13], 1.0 op_sel_hi:[1,0]
	v_pk_add_f32 v[14:15], v[14:15], v[78:79]
	v_pk_add_f32 v[14:15], v[14:15], 1.0 op_sel_hi:[1,0]
	v_pk_add_f32 v[16:17], v[16:17], v[80:81]
	v_pk_add_f32 v[16:17], v[16:17], 1.0 op_sel_hi:[1,0]
	v_pk_add_f32 v[18:19], v[18:19], v[82:83]
	v_pk_add_f32 v[18:19], v[18:19], 1.0 op_sel_hi:[1,0]
	v_pk_add_f32 v[20:21], v[20:21], v[84:85]
	v_pk_add_f32 v[20:21], v[20:21], 1.0 op_sel_hi:[1,0]
	v_pk_add_f32 v[22:23], v[22:23], v[86:87]
	v_pk_add_f32 v[22:23], v[22:23], 1.0 op_sel_hi:[1,0]
	v_pk_add_f32 v[24:25], v[24:25], v[88:89]
	v_pk_add_f32 v[24:25], v[24:25], 1.0 op_sel_hi:[1,0]
	v_pk_add_f32 v[26:27], v[26:27], v[90:91]
	v_pk_add_f32 v[26:27], v[26:27], 1.0 op_sel_hi:[1,0]
	v_pk_add_f32 v[28:29], v[28:29], v[92:93]
	v_pk_add_f32 v[28:29], v[28:29], 1.0 op_sel_hi:[1,0]
	v_pk_add_f32 v[30:31], v[30:31], v[94:95]
	v_pk_add_f32 v[30:31], v[30:31], 1.0 op_sel_hi:[1,0]
	v_pk_add_f32 v[32:33], v[32:33], v[96:97]
	v_pk_add_f32 v[32:33], v[32:33], 1.0 op_sel_hi:[1,0]
	v_pk_add_f32 v[34:35], v[34:35], v[98:99]
	v_pk_add_f32 v[34:35], v[34:35], 1.0 op_sel_hi:[1,0]
	v_pk_add_f32 v[36:37], v[36:37], v[100:101]
	v_pk_add_f32 v[36:37], v[36:37], 1.0 op_sel_hi:[1,0]
	v_pk_mul_f32 v[6:7], v[216:217], v[6:7]
	v_pk_mul_f32 v[8:9], v[218:219], v[8:9]
	v_pk_mul_f32 v[10:11], v[220:221], v[10:11]
	v_pk_mul_f32 v[12:13], v[222:223], v[12:13]
	v_pk_mul_f32 v[14:15], v[224:225], v[14:15]
	v_pk_mul_f32 v[16:17], v[226:227], v[16:17]
	v_pk_mul_f32 v[18:19], v[228:229], v[18:19]
	v_pk_mul_f32 v[20:21], v[230:231], v[20:21]
	v_pk_mul_f32 v[22:23], v[232:233], v[22:23]
	v_pk_mul_f32 v[24:25], v[234:235], v[24:25]
	v_pk_mul_f32 v[26:27], v[236:237], v[26:27]
	v_pk_mul_f32 v[28:29], v[238:239], v[28:29]
	v_pk_mul_f32 v[30:31], v[240:241], v[30:31]
	v_pk_mul_f32 v[32:33], v[242:243], v[32:33]
	v_pk_mul_f32 v[34:35], v[244:245], v[34:35]
	v_pk_mul_f32 v[36:37], v[246:247], v[36:37]
	v_pk_add_f32 v[38:39], v[38:39], v[176:177]
	v_pk_add_f32 v[40:41], v[40:41], v[178:179]
	v_pk_add_f32 v[42:43], v[42:43], v[180:181]
	v_pk_add_f32 v[44:45], v[44:45], v[182:183]
	v_pk_add_f32 v[46:47], v[46:47], v[184:185]
	v_pk_add_f32 v[48:49], v[48:49], v[186:187]
	v_pk_add_f32 v[50:51], v[50:51], v[188:189]
	v_pk_add_f32 v[52:53], v[52:53], v[190:191]
	v_pk_add_f32 v[54:55], v[54:55], v[192:193]
	v_pk_add_f32 v[56:57], v[56:57], v[194:195]
	v_pk_add_f32 v[58:59], v[58:59], v[196:197]
	v_pk_add_f32 v[60:61], v[60:61], v[198:199]
	v_pk_add_f32 v[62:63], v[62:63], v[162:163]
	v_pk_add_f32 v[64:65], v[64:65], v[164:165]
	v_pk_add_f32 v[66:67], v[66:67], v[166:167]
	v_pk_add_f32 v[68:69], v[68:69], v[168:169]
.Lpq_mod_ok_b:
	s_waitcnt vmcnt(8)
	v_lshlrev_b32_e32 v70, 16, v118
	v_and_b32_e32 v71, 0xffff0000, v118
	v_lshlrev_b32_e32 v72, 16, v119
	v_and_b32_e32 v73, 0xffff0000, v119
	v_lshlrev_b32_e32 v74, 16, v120
	v_and_b32_e32 v75, 0xffff0000, v120
	v_lshlrev_b32_e32 v76, 16, v121
	v_and_b32_e32 v77, 0xffff0000, v121
	v_lshlrev_b32_e32 v78, 16, v122
	v_and_b32_e32 v79, 0xffff0000, v122
	v_lshlrev_b32_e32 v80, 16, v123
	v_and_b32_e32 v81, 0xffff0000, v123
	v_lshlrev_b32_e32 v82, 16, v124
	v_and_b32_e32 v83, 0xffff0000, v124
	v_lshlrev_b32_e32 v84, 16, v125
	v_and_b32_e32 v85, 0xffff0000, v125
	v_lshlrev_b32_e32 v86, 16, v126
	v_and_b32_e32 v87, 0xffff0000, v126
	v_lshlrev_b32_e32 v88, 16, v127
	v_and_b32_e32 v89, 0xffff0000, v127
	v_lshlrev_b32_e32 v90, 16, v128
	v_and_b32_e32 v91, 0xffff0000, v128
	v_lshlrev_b32_e32 v92, 16, v129
	v_and_b32_e32 v93, 0xffff0000, v129
	v_lshlrev_b32_e32 v94, 16, v130
	v_and_b32_e32 v95, 0xffff0000, v130
	v_lshlrev_b32_e32 v96, 16, v131
	v_and_b32_e32 v97, 0xffff0000, v131
	v_lshlrev_b32_e32 v98, 16, v132
	v_and_b32_e32 v99, 0xffff0000, v132
	v_lshlrev_b32_e32 v100, 16, v133
	v_and_b32_e32 v101, 0xffff0000, v133
	s_add_u32 s18, s12, 2
	s_sub_u32 s19, s13, 1
	s_min_u32 s18, s18, s19
	s_lshl_b32 s16, s18, 12
	s_add_u32 s52, s38, s16
	s_addc_u32 s53, s39, 0
	global_load_dwordx4 v[118:121], v3, s[52:53]
	global_load_dwordx4 v[122:125], v3, s[52:53] offset:1024
	global_load_dwordx4 v[126:129], v3, s[52:53] offset:2048
	global_load_dwordx4 v[130:133], v3, s[52:53] offset:3072
	v_pk_mul_f32 v[136:137], v[70:71], v[70:71]
	v_pk_fma_f32 v[136:137], v[72:73], v[72:73], v[136:137]
	v_pk_fma_f32 v[136:137], v[74:75], v[74:75], v[136:137]
	v_pk_fma_f32 v[136:137], v[76:77], v[76:77], v[136:137]
	v_pk_fma_f32 v[136:137], v[78:79], v[78:79], v[136:137]
	v_pk_fma_f32 v[136:137], v[80:81], v[80:81], v[136:137]
	v_pk_fma_f32 v[136:137], v[82:83], v[82:83], v[136:137]
	v_pk_fma_f32 v[136:137], v[84:85], v[84:85], v[136:137]
	v_pk_fma_f32 v[136:137], v[86:87], v[86:87], v[136:137]
	v_pk_fma_f32 v[136:137], v[88:89], v[88:89], v[136:137]
	v_pk_fma_f32 v[136:137], v[90:91], v[90:91], v[136:137]
	v_pk_fma_f32 v[136:137], v[92:93], v[92:93], v[136:137]
	v_pk_fma_f32 v[136:137], v[94:95], v[94:95], v[136:137]
	v_pk_fma_f32 v[136:137], v[96:97], v[96:97], v[136:137]
	v_pk_fma_f32 v[136:137], v[98:99], v[98:99], v[136:137]
	v_pk_fma_f32 v[136:137], v[100:101], v[100:101], v[136:137]
	v_add_f32_e32 v136, v136, v137
	s_nop 1
	v_add_f32_dpp v136, v136, v136 quad_perm:[1,0,3,2] row_mask:0xf bank_mask:0xf bound_ctrl:1
	s_nop 1
	v_add_f32_dpp v136, v136, v136 quad_perm:[2,3,0,1] row_mask:0xf bank_mask:0xf bound_ctrl:1
	s_nop 1
	v_add_f32_dpp v136, v136, v136 row_half_mirror row_mask:0xf bank_mask:0xf bound_ctrl:1
	s_nop 1
	v_add_f32_dpp v136, v136, v136 row_mirror row_mask:0xf bank_mask:0xf bound_ctrl:1
	v_mov_b32_e32 v137, v136
	s_nop 1
	v_permlane16_swap_b32_e32 v136, v137
	v_add_f32_e32 v136, v136, v137
	v_mov_b32_e32 v137, v136
	s_nop 1
	v_permlane32_swap_b32_e32 v136, v137
	v_add_f32_e32 v136, v136, v137
	s_mov_b32 s17, 0x800000
	v_fmamk_f32 v136, v136, 0x3a000000, v212
	v_mul_f32_e32 v137, 0x4b800000, v136
	v_cmp_gt_f32_e32 vcc, s17, v136
	s_nop 1
	v_cndmask_b32_e32 v136, v136, v137, vcc
	v_rsq_f32_e32 v136, v136
	s_nop 0
	v_mul_f32_e32 v137, 0x45800000, v136
	v_cndmask_b32_e32 v136, v136, v137, vcc
	v_mov_b32_e32 v137, v136
	v_pk_mul_f32 v[70:71], v[70:71], v[136:137]
	v_pk_mul_f32 v[72:73], v[72:73], v[136:137]
	v_pk_mul_f32 v[74:75], v[74:75], v[136:137]
	v_pk_mul_f32 v[76:77], v[76:77], v[136:137]
	v_pk_mul_f32 v[78:79], v[78:79], v[136:137]
	v_pk_mul_f32 v[80:81], v[80:81], v[136:137]
	v_pk_mul_f32 v[82:83], v[82:83], v[136:137]
	v_pk_mul_f32 v[84:85], v[84:85], v[136:137]
	v_pk_mul_f32 v[86:87], v[86:87], v[136:137]
	v_pk_mul_f32 v[88:89], v[88:89], v[136:137]
	v_pk_mul_f32 v[90:91], v[90:91], v[136:137]
	v_pk_mul_f32 v[92:93], v[92:93], v[136:137]
	v_pk_mul_f32 v[94:95], v[94:95], v[136:137]
	v_pk_mul_f32 v[96:97], v[96:97], v[136:137]
	v_pk_mul_f32 v[98:99], v[98:99], v[136:137]
	v_pk_mul_f32 v[100:101], v[100:101], v[136:137]
	v_pk_fma_f32 v[70:71], v[70:71], v[6:7], v[38:39]
	v_pk_fma_f32 v[72:73], v[72:73], v[8:9], v[40:41]
	v_pk_fma_f32 v[74:75], v[74:75], v[10:11], v[42:43]
	v_pk_fma_f32 v[76:77], v[76:77], v[12:13], v[44:45]
	v_pk_fma_f32 v[78:79], v[78:79], v[14:15], v[46:47]
	v_pk_fma_f32 v[80:81], v[80:81], v[16:17], v[48:49]
	v_pk_fma_f32 v[82:83], v[82:83], v[18:19], v[50:51]
	v_pk_fma_f32 v[84:85], v[84:85], v[20:21], v[52:53]
	v_pk_fma_f32 v[86:87], v[86:87], v[22:23], v[54:55]
	v_pk_fma_f32 v[88:89], v[88:89], v[24:25], v[56:57]
	v_pk_fma_f32 v[90:91], v[90:91], v[26:27], v[58:59]
	v_pk_fma_f32 v[92:93], v[92:93], v[28:29], v[60:61]
	v_pk_fma_f32 v[94:95], v[94:95], v[30:31], v[62:63]
	v_pk_fma_f32 v[96:97], v[96:97], v[32:33], v[64:65]
	v_pk_fma_f32 v[98:99], v[98:99], v[34:35], v[66:67]
	v_pk_fma_f32 v[100:101], v[100:101], v[36:37], v[68:69]
	v_cvt_pk_bf16_f32 v70, v70, v71
	v_cvt_pk_bf16_f32 v71, v72, v73
	v_cvt_pk_bf16_f32 v72, v74, v75
	v_cvt_pk_bf16_f32 v73, v76, v77
	v_cvt_pk_bf16_f32 v78, v78, v79
	v_cvt_pk_bf16_f32 v79, v80, v81
	v_cvt_pk_bf16_f32 v80, v82, v83
	v_cvt_pk_bf16_f32 v81, v84, v85
	v_cvt_pk_bf16_f32 v86, v86, v87
	v_cvt_pk_bf16_f32 v87, v88, v89
	v_cvt_pk_bf16_f32 v88, v90, v91
	v_cvt_pk_bf16_f32 v89, v92, v93
	v_cvt_pk_bf16_f32 v94, v94, v95
	v_cvt_pk_bf16_f32 v95, v96, v97
	v_cvt_pk_bf16_f32 v96, v98, v99
	v_cvt_pk_bf16_f32 v97, v100, v101
	s_lshl_b32 s16, s12, 12
	s_add_u32 s52, s42, s16
	s_addc_u32 s53, s43, 0
	global_store_dwordx4 v3, v[70:73], s[52:53]
	global_store_dwordx4 v3, v[78:81], s[52:53] offset:1024
	global_store_dwordx4 v3, v[86:89], s[52:53] offset:2048
	global_store_dwordx4 v3, v[94:97], s[52:53] offset:3072
	s_add_u32 s12, s12, 1
	s_cmp_ge_u32 s12, s13
	s_cbranch_scc1 .Lpq_end
	s_lshr_b32 s16, s12, 12
	s_cmp_lt_u32 s12, 0x4000
	s_cselect_b32 s16, s16, 4
	s_cmp_eq_u32 s16, s15
	s_cbranch_scc1 .Lpq_mod_ok_c
	s_mov_b32 s15, s16
	s_mul_i32 s16, s16, 0xc000
	s_add_u32 s52, s46, s16
	s_addc_u32 s53, s47, 0
	s_add_u32 s10, s52, 0x8000
	s_addc_u32 s11, s53, 0
	s_add_u32 s52, s52, 0x6000
	s_addc_u32 s53, s53, 0
	s_add_u32 s16, s48, 0x8000
	s_addc_u32 s17, s49, 0
	s_add_u32 s18, s48, 0x6000
	s_addc_u32 s19, s49, 0
	global_load_dwordx4 v[6:9], v160, s[10:11]
	global_load_dwordx4 v[70:73], v160, s[16:17]
	global_load_dwordx4 v[38:41], v160, s[52:53]
	global_load_dwordx4 v[216:219], v160, s[50:51]
	global_load_dwordx4 v[176:179], v160, s[18:19]
	global_load_dwordx4 v[10:13], v160, s[10:11] offset:16
	global_load_dwordx4 v[74:77], v160, s[16:17] offset:16
	global_load_dwordx4 v[42:45], v160, s[52:53] offset:16
	global_load_dwordx4 v[220:223], v160, s[50:51] offset:16
	global_load_dwordx4 v[180:183], v160, s[18:19] offset:16
	global_load_dwordx4 v[14:17], v160, s[10:11] offset:2048
	global_load_dwordx4 v[78:81], v160, s[16:17] offset:2048
	global_load_dwordx4 v[46:49], v160, s[52:53] offset:2048
	global_load_dwordx4 v[224:227], v160, s[50:51] offset:2048
	global_load_dwordx4 v[184:187], v160, s[18:19] offset:2048
	global_load_dwordx4 v[18:21], v160, s[10:11] offset:2064
	global_load_dwordx4 v[82:85], v160, s[16:17] offset:2064
	global_load_dwordx4 v[50:53], v160, s[52:53] offset:2064
	global_load_dwordx4 v[228:231], v160, s[50:51] offset:2064
	global_load_dwordx4 v[188:191], v160, s[18:19] offset:2064
	global_load_dwordx4 v[22:25], v161, s[10:11]
	global_load_dwordx4 v[86:89], v161, s[16:17]
	global_load_dwordx4 v[54:57], v161, s[52:53]
	global_load_dwordx4 v[232:235], v161, s[50:51]
	global_load_dwordx4 v[192:195], v161, s[18:19]
	global_load_dwordx4 v[26:29], v161, s[10:11] offset:16
	global_load_dwordx4 v[90:93], v161, s[16:17] offset:16
	global_load_dwordx4 v[58:61], v161, s[52:53] offset:16
	global_load_dwordx4 v[236:239], v161, s[50:51] offset:16
	global_load_dwordx4 v[196:199], v161, s[18:19] offset:16
	global_load_dwordx4 v[30:33], v161, s[10:11] offset:2048
	global_load_dwordx4 v[94:97], v161, s[16:17] offset:2048
	global_load_dwordx4 v[62:65], v161, s[52:53] offset:2048
	global_load_dwordx4 v[240:243], v161, s[50:51] offset:2048
	global_load_dwordx4 v[162:165], v161, s[18:19] offset:2048
	global_load_dwordx4 v[34:37], v161, s[10:11] offset:2064
	global_load_dwordx4 v[98:101], v161, s[16:17] offset:2064
	global_load_dwordx4 v[66:69], v161, s[52:53] offset:2064
	global_load_dwordx4 v[244:247], v161, s[50:51] offset:2064
	global_load_dwordx4 v[166:169], v161, s[18:19] offset:2064
	s_waitcnt vmcnt(0)
	v_pk_add_f32 v[6:7], v[6:7], v[70:71]
	v_pk_add_f32 v[6:7], v[6:7], 1.0 op_sel_hi:[1,0]
	v_pk_add_f32 v[8:9], v[8:9], v[72:73]
	v_pk_add_f32 v[8:9], v[8:9], 1.0 op_sel_hi:[1,0]
	v_pk_add_f32 v[10:11], v[10:11], v[74:75]
	v_pk_add_f32 v[10:11], v[10:11], 1.0 op_sel_hi:[1,0]
	v_pk_add_f32 v[12:13], v[12:13], v[76:77]
	v_pk_add_f32 v[12:13], v[12:13], 1.0 op_sel_hi:[1,0]
	v_pk_add_f32 v[14:15], v[14:15], v[78:79]
	v_pk_add_f32 v[14:15], v[14:15], 1.0 op_sel_hi:[1,0]
	v_pk_add_f32 v[16:17], v[16:17], v[80:81]
	v_pk_add_f32 v[16:17], v[16:17], 1.0 op_sel_hi:[1,0]
	v_pk_add_f32 v[18:19], v[18:19], v[82:83]
	v_pk_add_f32 v[18:19], v[18:19], 1.0 op_sel_hi:[1,0]
	v_pk_add_f32 v[20:21], v[20:21], v[84:85]
	v_pk_add_f32 v[20:21], v[20:21], 1.0 op_sel_hi:[1,0]
	v_pk_add_f32 v[22:23], v[22:23], v[86:87]
	v_pk_add_f32 v[22:23], v[22:23], 1.0 op_sel_hi:[1,0]
	v_pk_add_f32 v[24:25], v[24:25], v[88:89]
	v_pk_add_f32 v[24:25], v[24:25], 1.0 op_sel_hi:[1,0]
	v_pk_add_f32 v[26:27], v[26:27], v[90:91]
	v_pk_add_f32 v[26:27], v[26:27], 1.0 op_sel_hi:[1,0]
	v_pk_add_f32 v[28:29], v[28:29], v[92:93]
	v_pk_add_f32 v[28:29], v[28:29], 1.0 op_sel_hi:[1,0]
	v_pk_add_f32 v[30:31], v[30:31], v[94:95]
	v_pk_add_f32 v[30:31], v[30:31], 1.0 op_sel_hi:[1,0]
	v_pk_add_f32 v[32:33], v[32:33], v[96:97]
	v_pk_add_f32 v[32:33], v[32:33], 1.0 op_sel_hi:[1,0]
	v_pk_add_f32 v[34:35], v[34:35], v[98:99]
	v_pk_add_f32 v[34:35], v[34:35], 1.0 op_sel_hi:[1,0]
	v_pk_add_f32 v[36:37], v[36:37], v[100:101]
	v_pk_add_f32 v[36:37], v[36:37], 1.0 op_sel_hi:[1,0]
	v_pk_mul_f32 v[6:7], v[216:217], v[6:7]
	v_pk_mul_f32 v[8:9], v[218:219], v[8:9]
	v_pk_mul_f32 v[10:11], v[220:221], v[10:11]
	v_pk_mul_f32 v[12:13], v[222:223], v[12:13]
	v_pk_mul_f32 v[14:15], v[224:225], v[14:15]
	v_pk_mul_f32 v[16:17], v[226:227], v[16:17]
	v_pk_mul_f32 v[18:19], v[228:229], v[18:19]
	v_pk_mul_f32 v[20:21], v[230:231], v[20:21]
	v_pk_mul_f32 v[22:23], v[232:233], v[22:23]
	v_pk_mul_f32 v[24:25], v[234:235], v[24:25]
	v_pk_mul_f32 v[26:27], v[236:237], v[26:27]
	v_pk_mul_f32 v[28:29], v[238:239], v[28:29]
	v_pk_mul_f32 v[30:31], v[240:241], v[30:31]
	v_pk_mul_f32 v[32:33], v[242:243], v[32:33]
	v_pk_mul_f32 v[34:35], v[244:245], v[34:35]
	v_pk_mul_f32 v[36:37], v[246:247], v[36:37]
	v_pk_add_f32 v[38:39], v[38:39], v[176:177]
	v_pk_add_f32 v[40:41], v[40:41], v[178:179]
	v_pk_add_f32 v[42:43], v[42:43], v[180:181]
	v_pk_add_f32 v[44:45], v[44:45], v[182:183]
	v_pk_add_f32 v[46:47], v[46:47], v[184:185]
	v_pk_add_f32 v[48:49], v[48:49], v[186:187]
	v_pk_add_f32 v[50:51], v[50:51], v[188:189]
	v_pk_add_f32 v[52:53], v[52:53], v[190:191]
	v_pk_add_f32 v[54:55], v[54:55], v[192:193]
	v_pk_add_f32 v[56:57], v[56:57], v[194:195]
	v_pk_add_f32 v[58:59], v[58:59], v[196:197]
	v_pk_add_f32 v[60:61], v[60:61], v[198:199]
	v_pk_add_f32 v[62:63], v[62:63], v[162:163]
	v_pk_add_f32 v[64:65], v[64:65], v[164:165]
	v_pk_add_f32 v[66:67], v[66:67], v[166:167]
	v_pk_add_f32 v[68:69], v[68:69], v[168:169]

.Lpn_setup_done:
	s_mov_b32 s15, -1
	s_lshl_b32 s16, s12, 12
	s_add_u32 s52, s38, s16
	s_addc_u32 s53, s39, 0
	global_load_dwordx4 v[102:105], v3, s[52:53]
	global_load_dwordx4 v[106:109], v3, s[52:53] offset:1024
	global_load_dwordx4 v[110:113], v3, s[52:53] offset:2048
	global_load_dwordx4 v[114:117], v3, s[52:53] offset:3072
	s_lshl_b32 s16, s12, 2
	s_add_u32 s52, s40, s16
	s_addc_u32 s53, s41, 0
	global_load_dword v134, v162, s[52:53]
	s_add_u32 s18, s12, 1
	s_min_u32 s18, s18, s13
	s_sub_u32 s19, s13, 1
	s_min_u32 s18, s18, s19
	s_lshl_b32 s16, s18, 12
	s_add_u32 s52, s38, s16
	s_addc_u32 s53, s39, 0
	global_load_dwordx4 v[118:121], v3, s[52:53]
	global_load_dwordx4 v[122:125], v3, s[52:53] offset:1024
	global_load_dwordx4 v[126:129], v3, s[52:53] offset:2048
	global_load_dwordx4 v[130:133], v3, s[52:53] offset:3072
	s_lshl_b32 s16, s18, 2
	s_add_u32 s52, s40, s16
	s_addc_u32 s53, s41, 0
	global_load_dword v135, v162, s[52:53]
	s_cmp_lg_u32 s14, 0
	s_cbranch_scc1 .Lpn_mod_ok_a
	s_lshr_b32 s16, s12, 12
	s_cmp_lt_u32 s12, 0x4000
	s_cselect_b32 s16, s16, 4
	s_cmp_eq_u32 s16, s15
	s_cbranch_scc1 .Lpn_mod_ok_a
	s_mov_b32 s15, s16
	s_mul_i32 s16, s16, 0xc000
	s_add_u32 s52, s46, s16
	s_addc_u32 s53, s47, 0
	s_add_u32 s10, s52, 0x2000
	s_addc_u32 s11, s53, 0
	s_add_u32 s16, s48, 0x2000
	s_addc_u32 s17, s49, 0
	global_load_dwordx4 v[6:9], v160, s[10:11]
	global_load_dwordx4 v[70:73], v160, s[16:17]
	global_load_dwordx4 v[38:41], v160, s[52:53]
	global_load_dwordx4 v[216:219], v160, s[50:51]
	global_load_dwordx4 v[176:179], v160, s[48:49]
	global_load_dwordx4 v[10:13], v160, s[10:11] offset:16
	global_load_dwordx4 v[74:77], v160, s[16:17] offset:16
	global_load_dwordx4 v[42:45], v160, s[52:53] offset:16
	global_load_dwordx4 v[220:223], v160, s[50:51] offset:16
	global_load_dwordx4 v[180:183], v160, s[48:49] offset:16
	global_load_dwordx4 v[14:17], v160, s[10:11] offset:2048
	global_load_dwordx4 v[78:81], v160, s[16:17] offset:2048
	global_load_dwordx4 v[46:49], v160, s[52:53] offset:2048
	global_load_dwordx4 v[224:227], v160, s[50:51] offset:2048
	global_load_dwordx4 v[184:187], v160, s[48:49] offset:2048
	global_load_dwordx4 v[18:21], v160, s[10:11] offset:2064
	global_load_dwordx4 v[82:85], v160, s[16:17] offset:2064
	global_load_dwordx4 v[50:53], v160, s[52:53] offset:2064
	global_load_dwordx4 v[228:231], v160, s[50:51] offset:2064
	global_load_dwordx4 v[188:191], v160, s[48:49] offset:2064
	global_load_dwordx4 v[22:25], v161, s[10:11]
	global_load_dwordx4 v[86:89], v161, s[16:17]
	global_load_dwordx4 v[54:57], v161, s[52:53]
	global_load_dwordx4 v[232:235], v161, s[50:51]
	global_load_dwordx4 v[192:195], v161, s[48:49]
	global_load_dwordx4 v[26:29], v161, s[10:11] offset:16
	global_load_dwordx4 v[90:93], v161, s[16:17] offset:16
	global_load_dwordx4 v[58:61], v161, s[52:53] offset:16
	global_load_dwordx4 v[236:239], v161, s[50:51] offset:16
	global_load_dwordx4 v[196:199], v161, s[48:49] offset:16
	global_load_dwordx4 v[30:33], v161, s[10:11] offset:2048
	global_load_dwordx4 v[94:97], v161, s[16:17] offset:2048
	global_load_dwordx4 v[62:65], v161, s[52:53] offset:2048
	global_load_dwordx4 v[240:243], v161, s[50:51] offset:2048
	global_load_dwordx4 v[164:167], v161, s[48:49] offset:2048
	global_load_dwordx4 v[34:37], v161, s[10:11] offset:2064
	global_load_dwordx4 v[98:101], v161, s[16:17] offset:2064
	global_load_dwordx4 v[66:69], v161, s[52:53] offset:2064
	global_load_dwordx4 v[244:247], v161, s[50:51] offset:2064
	global_load_dwordx4 v[168:171], v161, s[48:49] offset:2064
	s_waitcnt vmcnt(0)
	v_pk_add_f32 v[6:7], v[6:7], v[70:71]
	v_pk_add_f32 v[6:7], v[6:7], 1.0 op_sel_hi:[1,0]
	v_pk_add_f32 v[8:9], v[8:9], v[72:73]
	v_pk_add_f32 v[8:9], v[8:9], 1.0 op_sel_hi:[1,0]
	v_pk_add_f32 v[10:11], v[10:11], v[74:75]
	v_pk_add_f32 v[10:11], v[10:11], 1.0 op_sel_hi:[1,0]
	v_pk_add_f32 v[12:13], v[12:13], v[76:77]
	v_pk_add_f32 v[12:13], v[12:13], 1.0 op_sel_hi:[1,0]
	v_pk_add_f32 v[14:15], v[14:15], v[78:79]
	v_pk_add_f32 v[14:15], v[14:15], 1.0 op_sel_hi:[1,0]
	v_pk_add_f32 v[16:17], v[16:17], v[80:81]
	v_pk_add_f32 v[16:17], v[16:17], 1.0 op_sel_hi:[1,0]
	v_pk_add_f32 v[18:19], v[18:19], v[82:83]
	v_pk_add_f32 v[18:19], v[18:19], 1.0 op_sel_hi:[1,0]
	v_pk_add_f32 v[20:21], v[20:21], v[84:85]
	v_pk_add_f32 v[20:21], v[20:21], 1.0 op_sel_hi:[1,0]
	v_pk_add_f32 v[22:23], v[22:23], v[86:87]
	v_pk_add_f32 v[22:23], v[22:23], 1.0 op_sel_hi:[1,0]
	v_pk_add_f32 v[24:25], v[24:25], v[88:89]
	v_pk_add_f32 v[24:25], v[24:25], 1.0 op_sel_hi:[1,0]
	v_pk_add_f32 v[26:27], v[26:27], v[90:91]
	v_pk_add_f32 v[26:27], v[26:27], 1.0 op_sel_hi:[1,0]
	v_pk_add_f32 v[28:29], v[28:29], v[92:93]
	v_pk_add_f32 v[28:29], v[28:29], 1.0 op_sel_hi:[1,0]
	v_pk_add_f32 v[30:31], v[30:31], v[94:95]
	v_pk_add_f32 v[30:31], v[30:31], 1.0 op_sel_hi:[1,0]
	v_pk_add_f32 v[32:33], v[32:33], v[96:97]
	v_pk_add_f32 v[32:33], v[32:33], 1.0 op_sel_hi:[1,0]
	v_pk_add_f32 v[34:35], v[34:35], v[98:99]
	v_pk_add_f32 v[34:35], v[34:35], 1.0 op_sel_hi:[1,0]
	v_pk_add_f32 v[36:37], v[36:37], v[100:101]
	v_pk_add_f32 v[36:37], v[36:37], 1.0 op_sel_hi:[1,0]
	v_pk_mul_f32 v[6:7], v[216:217], v[6:7]
	v_pk_mul_f32 v[8:9], v[218:219], v[8:9]
	v_pk_mul_f32 v[10:11], v[220:221], v[10:11]
	v_pk_mul_f32 v[12:13], v[222:223], v[12:13]
	v_pk_mul_f32 v[14:15], v[224:225], v[14:15]
	v_pk_mul_f32 v[16:17], v[226:227], v[16:17]
	v_pk_mul_f32 v[18:19], v[228:229], v[18:19]
	v_pk_mul_f32 v[20:21], v[230:231], v[20:21]
	v_pk_mul_f32 v[22:23], v[232:233], v[22:23]
	v_pk_mul_f32 v[24:25], v[234:235], v[24:25]
	v_pk_mul_f32 v[26:27], v[236:237], v[26:27]
	v_pk_mul_f32 v[28:29], v[238:239], v[28:29]
	v_pk_mul_f32 v[30:31], v[240:241], v[30:31]
	v_pk_mul_f32 v[32:33], v[242:243], v[32:33]
	v_pk_mul_f32 v[34:35], v[244:245], v[34:35]
	v_pk_mul_f32 v[36:37], v[246:247], v[36:37]
	v_pk_add_f32 v[38:39], v[38:39], v[176:177]
	v_pk_add_f32 v[40:41], v[40:41], v[178:179]
	v_pk_add_f32 v[42:43], v[42:43], v[180:181]
	v_pk_add_f32 v[44:45], v[44:45], v[182:183]
	v_pk_add_f32 v[46:47], v[46:47], v[184:185]
	v_pk_add_f32 v[48:49], v[48:49], v[186:187]
	v_pk_add_f32 v[50:51], v[50:51], v[188:189]
	v_pk_add_f32 v[52:53], v[52:53], v[190:191]
	v_pk_add_f32 v[54:55], v[54:55], v[192:193]
	v_pk_add_f32 v[56:57], v[56:57], v[194:195]
	v_pk_add_f32 v[58:59], v[58:59], v[196:197]
	v_pk_add_f32 v[60:61], v[60:61], v[198:199]
	v_pk_add_f32 v[62:63], v[62:63], v[164:165]
	v_pk_add_f32 v[64:65], v[64:65], v[166:167]
	v_pk_add_f32 v[66:67], v[66:67], v[168:169]
	v_pk_add_f32 v[68:69], v[68:69], v[170:171]

.Lpn_loop:
	s_cmp_lg_u32 s14, 0
	s_cbranch_scc1 .Lpn_mod_ok_b
	s_lshr_b32 s16, s12, 12
	s_cmp_lt_u32 s12, 0x4000
	s_cselect_b32 s16, s16, 4
	s_cmp_eq_u32 s16, s15
	s_cbranch_scc1 .Lpn_mod_ok_b
	s_mov_b32 s15, s16
	s_mul_i32 s16, s16, 0xc000
	s_add_u32 s52, s46, s16
	s_addc_u32 s53, s47, 0
	s_add_u32 s10, s52, 0x2000
	s_addc_u32 s11, s53, 0
	s_add_u32 s16, s48, 0x2000
	s_addc_u32 s17, s49, 0
	global_load_dwordx4 v[6:9], v160, s[10:11]
	global_load_dwordx4 v[70:73], v160, s[16:17]
	global_load_dwordx4 v[38:41], v160, s[52:53]
	global_load_dwordx4 v[216:219], v160, s[50:51]
	global_load_dwordx4 v[176:179], v160, s[48:49]
	global_load_dwordx4 v[10:13], v160, s[10:11] offset:16
	global_load_dwordx4 v[74:77], v160, s[16:17] offset:16
	global_load_dwordx4 v[42:45], v160, s[52:53] offset:16
	global_load_dwordx4 v[220:223], v160, s[50:51] offset:16
	global_load_dwordx4 v[180:183], v160, s[48:49] offset:16
	global_load_dwordx4 v[14:17], v160, s[10:11] offset:2048
	global_load_dwordx4 v[78:81], v160, s[16:17] offset:2048
	global_load_dwordx4 v[46:49], v160, s[52:53] offset:2048
	global_load_dwordx4 v[224:227], v160, s[50:51] offset:2048
	global_load_dwordx4 v[184:187], v160, s[48:49] offset:2048
	global_load_dwordx4 v[18:21], v160, s[10:11] offset:2064
	global_load_dwordx4 v[82:85], v160, s[16:17] offset:2064
	global_load_dwordx4 v[50:53], v160, s[52:53] offset:2064
	global_load_dwordx4 v[228:231], v160, s[50:51] offset:2064
	global_load_dwordx4 v[188:191], v160, s[48:49] offset:2064
	global_load_dwordx4 v[22:25], v161, s[10:11]
	global_load_dwordx4 v[86:89], v161, s[16:17]
	global_load_dwordx4 v[54:57], v161, s[52:53]
	global_load_dwordx4 v[232:235], v161, s[50:51]
	global_load_dwordx4 v[192:195], v161, s[48:49]
	global_load_dwordx4 v[26:29], v161, s[10:11] offset:16
	global_load_dwordx4 v[90:93], v161, s[16:17] offset:16
	global_load_dwordx4 v[58:61], v161, s[52:53] offset:16
	global_load_dwordx4 v[236:239], v161, s[50:51] offset:16
	global_load_dwordx4 v[196:199], v161, s[48:49] offset:16
	global_load_dwordx4 v[30:33], v161, s[10:11] offset:2048
	global_load_dwordx4 v[94:97], v161, s[16:17] offset:2048
	global_load_dwordx4 v[62:65], v161, s[52:53] offset:2048
	global_load_dwordx4 v[240:243], v161, s[50:51] offset:2048
	global_load_dwordx4 v[164:167], v161, s[48:49] offset:2048
	global_load_dwordx4 v[34:37], v161, s[10:11] offset:2064
	global_load_dwordx4 v[98:101], v161, s[16:17] offset:2064
	global_load_dwordx4 v[66:69], v161, s[52:53] offset:2064
	global_load_dwordx4 v[244:247], v161, s[50:51] offset:2064
	global_load_dwordx4 v[168:171], v161, s[48:49] offset:2064
	s_waitcnt vmcnt(0)
	v_pk_add_f32 v[6:7], v[6:7], v[70:71]
	v_pk_add_f32 v[6:7], v[6:7], 1.0 op_sel_hi:[1,0]
	v_pk_add_f32 v[8:9], v[8:9], v[72:73]
	v_pk_add_f32 v[8:9], v[8:9], 1.0 op_sel_hi:[1,0]
	v_pk_add_f32 v[10:11], v[10:11], v[74:75]
	v_pk_add_f32 v[10:11], v[10:11], 1.0 op_sel_hi:[1,0]
	v_pk_add_f32 v[12:13], v[12:13], v[76:77]
	v_pk_add_f32 v[12:13], v[12:13], 1.0 op_sel_hi:[1,0]
	v_pk_add_f32 v[14:15], v[14:15], v[78:79]
	v_pk_add_f32 v[14:15], v[14:15], 1.0 op_sel_hi:[1,0]
	v_pk_add_f32 v[16:17], v[16:17], v[80:81]
	v_pk_add_f32 v[16:17], v[16:17], 1.0 op_sel_hi:[1,0]
	v_pk_add_f32 v[18:19], v[18:19], v[82:83]
	v_pk_add_f32 v[18:19], v[18:19], 1.0 op_sel_hi:[1,0]
	v_pk_add_f32 v[20:21], v[20:21], v[84:85]
	v_pk_add_f32 v[20:21], v[20:21], 1.0 op_sel_hi:[1,0]
	v_pk_add_f32 v[22:23], v[22:23], v[86:87]
	v_pk_add_f32 v[22:23], v[22:23], 1.0 op_sel_hi:[1,0]
	v_pk_add_f32 v[24:25], v[24:25], v[88:89]
	v_pk_add_f32 v[24:25], v[24:25], 1.0 op_sel_hi:[1,0]
	v_pk_add_f32 v[26:27], v[26:27], v[90:91]
	v_pk_add_f32 v[26:27], v[26:27], 1.0 op_sel_hi:[1,0]
	v_pk_add_f32 v[28:29], v[28:29], v[92:93]
	v_pk_add_f32 v[28:29], v[28:29], 1.0 op_sel_hi:[1,0]
	v_pk_add_f32 v[30:31], v[30:31], v[94:95]
	v_pk_add_f32 v[30:31], v[30:31], 1.0 op_sel_hi:[1,0]
	v_pk_add_f32 v[32:33], v[32:33], v[96:97]
	v_pk_add_f32 v[32:33], v[32:33], 1.0 op_sel_hi:[1,0]
	v_pk_add_f32 v[34:35], v[34:35], v[98:99]
	v_pk_add_f32 v[34:35], v[34:35], 1.0 op_sel_hi:[1,0]
	v_pk_add_f32 v[36:37], v[36:37], v[100:101]
	v_pk_add_f32 v[36:37], v[36:37], 1.0 op_sel_hi:[1,0]
	v_pk_mul_f32 v[6:7], v[216:217], v[6:7]
	v_pk_mul_f32 v[8:9], v[218:219], v[8:9]
	v_pk_mul_f32 v[10:11], v[220:221], v[10:11]
	v_pk_mul_f32 v[12:13], v[222:223], v[12:13]
	v_pk_mul_f32 v[14:15], v[224:225], v[14:15]
	v_pk_mul_f32 v[16:17], v[226:227], v[16:17]
	v_pk_mul_f32 v[18:19], v[228:229], v[18:19]
	v_pk_mul_f32 v[20:21], v[230:231], v[20:21]
	v_pk_mul_f32 v[22:23], v[232:233], v[22:23]
	v_pk_mul_f32 v[24:25], v[234:235], v[24:25]
	v_pk_mul_f32 v[26:27], v[236:237], v[26:27]
	v_pk_mul_f32 v[28:29], v[238:239], v[28:29]
	v_pk_mul_f32 v[30:31], v[240:241], v[30:31]
	v_pk_mul_f32 v[32:33], v[242:243], v[32:33]
	v_pk_mul_f32 v[34:35], v[244:245], v[34:35]
	v_pk_mul_f32 v[36:37], v[246:247], v[36:37]
	v_pk_add_f32 v[38:39], v[38:39], v[176:177]
	v_pk_add_f32 v[40:41], v[40:41], v[178:179]
	v_pk_add_f32 v[42:43], v[42:43], v[180:181]
	v_pk_add_f32 v[44:45], v[44:45], v[182:183]
	v_pk_add_f32 v[46:47], v[46:47], v[184:185]
	v_pk_add_f32 v[48:49], v[48:49], v[186:187]
	v_pk_add_f32 v[50:51], v[50:51], v[188:189]
	v_pk_add_f32 v[52:53], v[52:53], v[190:191]
	v_pk_add_f32 v[54:55], v[54:55], v[192:193]
	v_pk_add_f32 v[56:57], v[56:57], v[194:195]
	v_pk_add_f32 v[58:59], v[58:59], v[196:197]
	v_pk_add_f32 v[60:61], v[60:61], v[198:199]
	v_pk_add_f32 v[62:63], v[62:63], v[164:165]
	v_pk_add_f32 v[64:65], v[64:65], v[166:167]
	v_pk_add_f32 v[66:67], v[66:67], v[168:169]
	v_pk_add_f32 v[68:69], v[68:69], v[170:171]

.Lpn_next_b:
	s_add_u32 s12, s12, 1
	s_cmp_ge_u32 s12, s13
	s_cbranch_scc1 .Lpn_end
	s_cmp_lg_u32 s14, 0
	s_cbranch_scc1 .Lpn_mod_ok_c
	s_lshr_b32 s16, s12, 12
	s_cmp_lt_u32 s12, 0x4000
	s_cselect_b32 s16, s16, 4
	s_cmp_eq_u32 s16, s15
	s_cbranch_scc1 .Lpn_mod_ok_c
	s_mov_b32 s15, s16
	s_mul_i32 s16, s16, 0xc000
	s_add_u32 s52, s46, s16
	s_addc_u32 s53, s47, 0
	s_add_u32 s10, s52, 0x2000
	s_addc_u32 s11, s53, 0
	s_add_u32 s16, s48, 0x2000
	s_addc_u32 s17, s49, 0
	global_load_dwordx4 v[6:9], v160, s[10:11]
	global_load_dwordx4 v[70:73], v160, s[16:17]
	global_load_dwordx4 v[38:41], v160, s[52:53]
	global_load_dwordx4 v[216:219], v160, s[50:51]
	global_load_dwordx4 v[176:179], v160, s[48:49]
	global_load_dwordx4 v[10:13], v160, s[10:11] offset:16
	global_load_dwordx4 v[74:77], v160, s[16:17] offset:16
	global_load_dwordx4 v[42:45], v160, s[52:53] offset:16
	global_load_dwordx4 v[220:223], v160, s[50:51] offset:16
	global_load_dwordx4 v[180:183], v160, s[48:49] offset:16
	global_load_dwordx4 v[14:17], v160, s[10:11] offset:2048
	global_load_dwordx4 v[78:81], v160, s[16:17] offset:2048
	global_load_dwordx4 v[46:49], v160, s[52:53] offset:2048
	global_load_dwordx4 v[224:227], v160, s[50:51] offset:2048
	global_load_dwordx4 v[184:187], v160, s[48:49] offset:2048
	global_load_dwordx4 v[18:21], v160, s[10:11] offset:2064
	global_load_dwordx4 v[82:85], v160, s[16:17] offset:2064
	global_load_dwordx4 v[50:53], v160, s[52:53] offset:2064
	global_load_dwordx4 v[228:231], v160, s[50:51] offset:2064
	global_load_dwordx4 v[188:191], v160, s[48:49] offset:2064
	global_load_dwordx4 v[22:25], v161, s[10:11]
	global_load_dwordx4 v[86:89], v161, s[16:17]
	global_load_dwordx4 v[54:57], v161, s[52:53]
	global_load_dwordx4 v[232:235], v161, s[50:51]
	global_load_dwordx4 v[192:195], v161, s[48:49]
	global_load_dwordx4 v[26:29], v161, s[10:11] offset:16
	global_load_dwordx4 v[90:93], v161, s[16:17] offset:16
	global_load_dwordx4 v[58:61], v161, s[52:53] offset:16
	global_load_dwordx4 v[236:239], v161, s[50:51] offset:16
	global_load_dwordx4 v[196:199], v161, s[48:49] offset:16
	global_load_dwordx4 v[30:33], v161, s[10:11] offset:2048
	global_load_dwordx4 v[94:97], v161, s[16:17] offset:2048
	global_load_dwordx4 v[62:65], v161, s[52:53] offset:2048
	global_load_dwordx4 v[240:243], v161, s[50:51] offset:2048
	global_load_dwordx4 v[164:167], v161, s[48:49] offset:2048
	global_load_dwordx4 v[34:37], v161, s[10:11] offset:2064
	global_load_dwordx4 v[98:101], v161, s[16:17] offset:2064
	global_load_dwordx4 v[66:69], v161, s[52:53] offset:2064
	global_load_dwordx4 v[244:247], v161, s[50:51] offset:2064
	global_load_dwordx4 v[168:171], v161, s[48:49] offset:2064
	s_waitcnt vmcnt(0)
	v_pk_add_f32 v[6:7], v[6:7], v[70:71]
	v_pk_add_f32 v[6:7], v[6:7], 1.0 op_sel_hi:[1,0]
	v_pk_add_f32 v[8:9], v[8:9], v[72:73]
	v_pk_add_f32 v[8:9], v[8:9], 1.0 op_sel_hi:[1,0]
	v_pk_add_f32 v[10:11], v[10:11], v[74:75]
	v_pk_add_f32 v[10:11], v[10:11], 1.0 op_sel_hi:[1,0]
	v_pk_add_f32 v[12:13], v[12:13], v[76:77]
	v_pk_add_f32 v[12:13], v[12:13], 1.0 op_sel_hi:[1,0]
	v_pk_add_f32 v[14:15], v[14:15], v[78:79]
	v_pk_add_f32 v[14:15], v[14:15], 1.0 op_sel_hi:[1,0]
	v_pk_add_f32 v[16:17], v[16:17], v[80:81]
	v_pk_add_f32 v[16:17], v[16:17], 1.0 op_sel_hi:[1,0]
	v_pk_add_f32 v[18:19], v[18:19], v[82:83]
	v_pk_add_f32 v[18:19], v[18:19], 1.0 op_sel_hi:[1,0]
	v_pk_add_f32 v[20:21], v[20:21], v[84:85]
	v_pk_add_f32 v[20:21], v[20:21], 1.0 op_sel_hi:[1,0]
	v_pk_add_f32 v[22:23], v[22:23], v[86:87]
	v_pk_add_f32 v[22:23], v[22:23], 1.0 op_sel_hi:[1,0]
	v_pk_add_f32 v[24:25], v[24:25], v[88:89]
	v_pk_add_f32 v[24:25], v[24:25], 1.0 op_sel_hi:[1,0]
	v_pk_add_f32 v[26:27], v[26:27], v[90:91]
	v_pk_add_f32 v[26:27], v[26:27], 1.0 op_sel_hi:[1,0]
	v_pk_add_f32 v[28:29], v[28:29], v[92:93]
	v_pk_add_f32 v[28:29], v[28:29], 1.0 op_sel_hi:[1,0]
	v_pk_add_f32 v[30:31], v[30:31], v[94:95]
	v_pk_add_f32 v[30:31], v[30:31], 1.0 op_sel_hi:[1,0]
	v_pk_add_f32 v[32:33], v[32:33], v[96:97]
	v_pk_add_f32 v[32:33], v[32:33], 1.0 op_sel_hi:[1,0]
	v_pk_add_f32 v[34:35], v[34:35], v[98:99]
	v_pk_add_f32 v[34:35], v[34:35], 1.0 op_sel_hi:[1,0]
	v_pk_add_f32 v[36:37], v[36:37], v[100:101]
	v_pk_add_f32 v[36:37], v[36:37], 1.0 op_sel_hi:[1,0]
	v_pk_mul_f32 v[6:7], v[216:217], v[6:7]
	v_pk_mul_f32 v[8:9], v[218:219], v[8:9]
	v_pk_mul_f32 v[10:11], v[220:221], v[10:11]
	v_pk_mul_f32 v[12:13], v[222:223], v[12:13]
	v_pk_mul_f32 v[14:15], v[224:225], v[14:15]
	v_pk_mul_f32 v[16:17], v[226:227], v[16:17]
	v_pk_mul_f32 v[18:19], v[228:229], v[18:19]
	v_pk_mul_f32 v[20:21], v[230:231], v[20:21]
	v_pk_mul_f32 v[22:23], v[232:233], v[22:23]
	v_pk_mul_f32 v[24:25], v[234:235], v[24:25]
	v_pk_mul_f32 v[26:27], v[236:237], v[26:27]
	v_pk_mul_f32 v[28:29], v[238:239], v[28:29]
	v_pk_mul_f32 v[30:31], v[240:241], v[30:31]
	v_pk_mul_f32 v[32:33], v[242:243], v[32:33]
	v_pk_mul_f32 v[34:35], v[244:245], v[34:35]
	v_pk_mul_f32 v[36:37], v[246:247], v[36:37]
	v_pk_add_f32 v[38:39], v[38:39], v[176:177]
	v_pk_add_f32 v[40:41], v[40:41], v[178:179]
	v_pk_add_f32 v[42:43], v[42:43], v[180:181]
	v_pk_add_f32 v[44:45], v[44:45], v[182:183]
	v_pk_add_f32 v[46:47], v[46:47], v[184:185]
	v_pk_add_f32 v[48:49], v[48:49], v[186:187]
	v_pk_add_f32 v[50:51], v[50:51], v[188:189]
	v_pk_add_f32 v[52:53], v[52:53], v[190:191]
	v_pk_add_f32 v[54:55], v[54:55], v[192:193]
	v_pk_add_f32 v[56:57], v[56:57], v[194:195]
	v_pk_add_f32 v[58:59], v[58:59], v[196:197]
	v_pk_add_f32 v[60:61], v[60:61], v[198:199]
	v_pk_add_f32 v[62:63], v[62:63], v[164:165]
	v_pk_add_f32 v[64:65], v[64:65], v[166:167]
	v_pk_add_f32 v[66:67], v[66:67], v[168:169]
	v_pk_add_f32 v[68:69], v[68:69], v[170:171]
